# v9_qhoist
# speedup vs baseline: 1.0713x; 1.0079x over previous
.LBB1_53:
	ds_read_b128 v[164:167], v205 offset:43008
	ds_read_b128 v[168:171], v205 offset:43040
	ds_read_b128 v[172:175], v205 offset:43072
	ds_read_b128 v[176:179], v205 offset:43104
	ds_read_b128 v[180:183], v205 offset:43136
	ds_read_b128 v[184:187], v205 offset:43168
	ds_read_b128 v[188:191], v205 offset:43200
	ds_read_b128 v[192:195], v205 offset:43232
	s_waitcnt vmcnt(17) lgkmcnt(7)
	v_mfma_f32_32x32x16_f16 v[34:49], v[112:115], v[164:167], 0
	s_waitcnt vmcnt(0)
	v_mfma_f32_32x32x16_f16 v[18:33], v[116:119], v[164:167], v[2:17]
	s_waitcnt lgkmcnt(6)
	v_mfma_f32_32x32x16_f16 v[34:49], v[100:103], v[168:171], v[34:49]
	v_mfma_f32_32x32x16_f16 v[18:33], v[120:123], v[168:171], v[18:33]
	s_waitcnt lgkmcnt(5)
	v_mfma_f32_32x32x16_f16 v[34:49], v[104:107], v[172:175], v[34:49]
	v_mfma_f32_32x32x16_f16 v[18:33], v[124:127], v[172:175], v[18:33]
	s_waitcnt lgkmcnt(4)
	v_mfma_f32_32x32x16_f16 v[34:49], v[108:111], v[176:179], v[34:49]
	v_mfma_f32_32x32x16_f16 v[18:33], v[128:131], v[176:179], v[18:33]
	s_waitcnt lgkmcnt(3)
	v_mfma_f32_32x32x16_f16 v[34:49], v[132:135], v[180:183], v[34:49]
	v_mfma_f32_32x32x16_f16 v[18:33], v[148:151], v[180:183], v[18:33]
	s_waitcnt lgkmcnt(2)
	v_mfma_f32_32x32x16_f16 v[34:49], v[136:139], v[184:187], v[34:49]
	v_mfma_f32_32x32x16_f16 v[18:33], v[152:155], v[184:187], v[18:33]
	s_waitcnt lgkmcnt(1)
	v_mfma_f32_32x32x16_f16 v[34:49], v[140:143], v[188:191], v[34:49]
	v_mfma_f32_32x32x16_f16 v[18:33], v[156:159], v[188:191], v[18:33]
	s_waitcnt lgkmcnt(0)
	v_mfma_f32_32x32x16_f16 v[34:49], v[144:147], v[192:195], v[34:49]
	v_mfma_f32_32x32x16_f16 v[18:33], v[160:163], v[192:195], v[18:33]
	s_nop 10
	v_cvt_pk_f16_f32 v41, v40, v41
	v_cvt_pk_f16_f32 v40, v38, v39
	v_cvt_pk_f16_f32 v39, v36, v37
	v_cvt_pk_f16_f32 v38, v34, v35
	v_cvt_pk_f16_f32 v25, v24, v25
	v_cvt_pk_f16_f32 v24, v22, v23
	v_cvt_pk_f16_f32 v23, v20, v21
	v_cvt_pk_f16_f32 v22, v18, v19
	v_cvt_pk_f16_f32 v21, v48, v49
	v_cvt_pk_f16_f32 v20, v46, v47
	v_cvt_pk_f16_f32 v19, v44, v45
	v_cvt_pk_f16_f32 v18, v42, v43
	v_mfma_f32_32x32x16_f16 v[50:65], v[38:41], v[22:25], 0
	v_cvt_pk_f16_f32 v25, v32, v33
	v_cvt_pk_f16_f32 v24, v30, v31
	v_cvt_pk_f16_f32 v23, v28, v29
	v_cvt_pk_f16_f32 v22, v26, v27
	s_nop 1
	v_mfma_f32_32x32x16_f16 v[34:49], v[18:21], v[22:25], 0
	v_mfma_f32_32x32x16_f16 v[18:33], v[164:167], v[96:99], 0
	v_mfma_f32_32x32x16_f16 v[18:33], v[168:171], v[76:79], v[18:33]
	s_nop 2
	v_max3_f32 v46, v50, v51, v52
	v_max3_f32 v46, v46, v53, v54
	v_max3_f32 v46, v46, v55, v56
	v_max_f32_e32 v47, v61, v61
	v_max_f32_e32 v48, v60, v60
	v_max3_f32 v46, v46, v57, v58
	v_max_f32_e32 v47, v48, v47
	v_mfma_f32_32x32x16_f16 v[18:33], v[172:175], v[72:75], v[18:33]
	v_max3_f32 v47, v46, v59, v47
	v_cndmask_b32_e64 v46, v46, v47, s[0:1]
	v_mov_b32_e32 v47, v46
	s_nop 1
	v_permlane32_swap_b32_e32 v46, v47
	v_max_f32_e32 v47, v47, v47
	v_max_f32_e32 v46, v46, v46
	v_max_f32_e32 v46, v46, v47
	v_mfma_f32_32x32x16_f16 v[18:33], v[176:179], v[68:71], v[18:33]
	v_sub_f32_e32 v47, v50, v46
	v_exp_f32_e32 v50, v47
	v_sub_f32_e32 v47, v51, v46
	v_sub_f32_e32 v48, v52, v46
	v_exp_f32_e32 v51, v47
	v_exp_f32_e32 v52, v48
	v_sub_f32_e32 v48, v53, v46
	v_sub_f32_e32 v49, v55, v46
	v_mfma_f32_32x32x16_f16 v[18:33], v[180:183], v[92:95], v[18:33]
	v_sub_f32_e32 v53, v57, v46
	v_exp_f32_e32 v55, v49
	v_sub_f32_e32 v49, v56, v46
	v_exp_f32_e32 v56, v53
	v_sub_f32_e32 v53, v58, v46
	v_exp_f32_e32 v62, v48
	v_sub_f32_e32 v48, v54, v46
	v_exp_f32_e32 v57, v53
	v_mfma_f32_32x32x16_f16 v[18:33], v[184:187], v[84:87], v[18:33]
	v_sub_f32_e32 v53, v59, v46
	v_add_f32_e32 v47, 0, v50
	v_exp_f32_e32 v48, v48
	v_exp_f32_e32 v53, v53
	v_add_f32_e32 v47, v51, v47
	v_add_f32_e32 v47, v52, v47
	v_exp_f32_e32 v49, v49
	v_add_f32_e32 v47, v62, v47
	v_mfma_f32_32x32x16_f16 v[18:33], v[188:191], v[88:91], v[18:33]
	v_add_f32_e32 v47, v48, v47
	v_cndmask_b32_e64 v58, v53, 0, s[14:15]
	v_sub_f32_e32 v53, v60, v46
	v_sub_f32_e32 v46, v61, v46
	v_add_f32_e32 v47, v55, v47
	v_exp_f32_e32 v53, v53
	v_exp_f32_e32 v46, v46
	v_add_f32_e32 v47, v49, v47
	v_mfma_f32_32x32x16_f16 v[18:33], v[192:195], v[80:83], v[18:33]
	ds_read_b128 v[192:195], v240 offset:48720
	ds_read_b128 v[188:191], v240 offset:48752
	ds_read_b128 v[184:187], v240 offset:48784
	ds_read_b128 v[180:183], v240 offset:48816
	ds_read_b128 v[176:179], v240 offset:48848
	ds_read_b128 v[172:175], v240 offset:48880
	ds_read_b128 v[168:171], v240 offset:48912
	ds_read_b128 v[164:167], v240 offset:48944
	v_add_f32_e32 v47, v56, v47
	v_add_f32_e32 v47, v57, v47
	v_add_f32_e32 v47, v58, v47
	v_cndmask_b32_e64 v59, v53, 0, s[14:15]
	v_cndmask_b32_e64 v60, v46, 0, s[14:15]
	v_cvt_pk_f16_f32 v46, v50, v51
	v_max3_f32 v50, v34, v35, v36
	v_add_f32_e32 v47, v59, v47
	v_max3_f32 v50, v50, v37, v38
	v_add_f32_e32 v53, v60, v47
	v_cvt_pk_f16_f32 v47, v52, v62
	v_max3_f32 v50, v50, v39, v40
	v_max_f32_e32 v51, v45, v45
	v_max_f32_e32 v52, v44, v44
	v_max3_f32 v50, v50, v41, v42
	v_max_f32_e32 v51, v52, v51
	v_max3_f32 v51, v50, v43, v51
	v_cndmask_b32_e64 v50, v50, v51, s[0:1]
	v_mov_b32_e32 v51, v50
	s_nop 1
	v_permlane32_swap_b32_e32 v50, v51
	s_waitcnt lgkmcnt(7)
	v_mfma_f32_32x32x16_f16 v[2:17], v[116:119], v[192:195], v[2:17]
	v_max_f32_e32 v51, v51, v51
	v_max_f32_e32 v50, v50, v50
	v_max_f32_e32 v50, v50, v51
	v_sub_f32_e32 v34, v34, v50
	v_exp_f32_e32 v52, v34
	v_sub_f32_e32 v34, v35, v50
	v_sub_f32_e32 v35, v36, v50
	s_waitcnt lgkmcnt(6)
	v_mfma_f32_32x32x16_f16 v[2:17], v[120:123], v[188:191], v[2:17]
	v_cvt_pk_f16_f32 v49, v49, v56
	v_exp_f32_e32 v56, v35
	v_sub_f32_e32 v35, v37, v50
	v_cvt_pk_f16_f32 v64, v57, v58
	v_exp_f32_e32 v57, v35
	v_sub_f32_e32 v35, v38, v50
	v_exp_f32_e32 v58, v35
	s_waitcnt lgkmcnt(5)
	v_mfma_f32_32x32x16_f16 v[2:17], v[124:127], v[184:187], v[2:17]
	v_sub_f32_e32 v35, v39, v50
	v_cvt_pk_f16_f32 v65, v59, v60
	v_exp_f32_e32 v60, v35
	v_sub_f32_e32 v35, v40, v50
	v_cvt_pk_f16_f32 v48, v48, v55
	v_exp_f32_e32 v55, v34
	v_exp_f32_e32 v62, v35
	s_waitcnt lgkmcnt(4)
	v_mfma_f32_32x32x16_f16 v[2:17], v[128:131], v[180:183], v[2:17]
	v_sub_f32_e32 v35, v41, v50
	v_exp_f32_e32 v63, v35
	v_sub_f32_e32 v35, v42, v50
	v_exp_f32_e32 v59, v35
	v_sub_f32_e32 v35, v43, v50
	v_add_f32_e32 v34, 0, v52
	v_exp_f32_e32 v35, v35
	s_waitcnt lgkmcnt(3)
	v_mfma_f32_32x32x16_f16 v[2:17], v[148:151], v[176:179], v[2:17]
	v_add_f32_e32 v34, v55, v34
	v_add_f32_e32 v34, v56, v34
	v_add_f32_e32 v34, v57, v34
	v_add_f32_e32 v34, v58, v34
	v_cndmask_b32_e64 v61, v35, 0, s[14:15]
	v_sub_f32_e32 v35, v44, v50
	v_add_f32_e32 v34, v60, v34
	s_waitcnt lgkmcnt(2)
	v_mfma_f32_32x32x16_f16 v[2:17], v[152:155], v[172:175], v[2:17]
	v_exp_f32_e32 v35, v35
	v_sub_f32_e32 v36, v45, v50
	v_cvt_pk_f16_f32 v25, v24, v25
	v_cvt_pk_f16_f32 v24, v22, v23
	v_cvt_pk_f16_f32 v23, v20, v21
	v_cvt_pk_f16_f32 v22, v18, v19
	v_add_f32_e32 v34, v62, v34
	s_waitcnt lgkmcnt(1)
	v_mfma_f32_32x32x16_f16 v[2:17], v[156:159], v[168:171], v[2:17]
	v_exp_f32_e32 v36, v36
	v_add_f32_e32 v34, v63, v34
	v_add_f32_e32 v34, v59, v34
	v_add_f32_e32 v34, v61, v34
	v_cndmask_b32_e64 v211, v35, 0, s[14:15]
	v_add_f32_e32 v18, v211, v34
	s_waitcnt lgkmcnt(0)
	v_mfma_f32_32x32x16_f16 v[2:17], v[160:163], v[164:167], v[2:17]
	v_cndmask_b32_e64 v250, v36, 0, s[14:15]
	v_cvt_pk_f16_f32 v51, v32, v33
	v_mfma_f32_32x32x16_f16 v[32:47], v[22:25], v[46:49], 0
	v_cvt_pk_f16_f32 v50, v30, v31
	v_cvt_pk_f16_f32 v49, v28, v29
	v_cvt_pk_f16_f32 v48, v26, v27
	v_mov_b32_e32 v67, v66
	v_add_f32_e32 v251, v250, v18
	v_mov_b32_e32 v54, v53
	v_mov_b32_e32 v252, v251
	v_mfma_f32_32x32x16_f16 v[32:47], v[48:51], v[64:67], v[32:47]
	v_permlane32_swap_b32_e32 v53, v54
	v_permlane32_swap_b32_e32 v251, v252
	s_and_saveexec_b64 s[2:3], s[4:5]
	s_cbranch_execz .LBB1_55
	v_add_f32_e32 v18, v53, v54
	v_rcp_f32_e32 v18, v18
	s_nop 5
	v_mov_b32_e32 v20, v33
	v_mov_b32_e32 v21, v34
	v_mov_b32_e32 v26, v37
	v_fma_mixlo_f16 v19, v18, v32, 0
	v_pk_mul_f32 v[20:21], v[18:19], v[20:21] op_sel_hi:[0,1]
	v_mov_b32_e32 v27, v38
	v_cvt_pk_f16_f32 v21, v20, v21
	v_pk_mul_f32 v[26:27], v[18:19], v[26:27] op_sel_hi:[0,1]
	v_fma_mixlo_f16 v28, v18, v36, 0
	v_pack_b32_f16 v20, v19, v21
	v_cvt_pk_f16_f32 v19, v26, v27
	v_fma_mixlo_f16 v27, v18, v35, 0
	v_fma_mixlo_f16 v18, v18, v39, 0
	v_pack_b32_f16 v26, v28, v19
	v_alignbit_b32 v21, v27, v21, 16
	v_alignbit_b32 v27, v18, v19, 16
	ds_write2_b64 v247, v[20:21], v[26:27] offset1:2

.LBB1_57:
	s_or_b64 exec, exec, s[2:3]
	s_waitcnt lgkmcnt(7)
	v_mfma_f32_32x32x16_f16 v[18:33], v[112:115], v[192:195], 0
	s_lshl_b64 s[2:3], s[36:37], 15
	v_lshl_add_u64 v[34:35], v[208:209], 0, s[2:3]
	s_waitcnt lgkmcnt(6)
	v_mfma_f32_32x32x16_f16 v[18:33], v[100:103], v[188:191], v[18:33]
	global_load_dwordx4 v[100:103], v[34:35], off
	global_load_dwordx4 v[58:61], v[34:35], off offset:1024
	global_load_dwordx4 v[54:57], v[34:35], off offset:2048
	global_load_dwordx4 v[50:53], v[34:35], off offset:3072
	s_waitcnt lgkmcnt(5)
	v_mfma_f32_32x32x16_f16 v[18:33], v[104:107], v[184:187], v[18:33]
	s_waitcnt lgkmcnt(4)
	v_mfma_f32_32x32x16_f16 v[18:33], v[108:111], v[180:183], v[18:33]
	s_waitcnt lgkmcnt(3)
	v_mfma_f32_32x32x16_f16 v[18:33], v[132:135], v[176:179], v[18:33]
	s_waitcnt lgkmcnt(2)
	v_mfma_f32_32x32x16_f16 v[18:33], v[136:139], v[172:175], v[18:33]
	s_waitcnt lgkmcnt(1)
	v_mfma_f32_32x32x16_f16 v[18:33], v[140:143], v[168:171], v[18:33]
	s_waitcnt lgkmcnt(0)
	v_mfma_f32_32x32x16_f16 v[18:33], v[144:147], v[164:167], v[18:33]
	s_nop 11
	v_cvt_pk_f16_f32 v25, v24, v25
	v_cvt_pk_f16_f32 v24, v22, v23
	v_cvt_pk_f16_f32 v23, v20, v21
	v_cvt_pk_f16_f32 v22, v18, v19
	v_cvt_pk_f16_f32 v9, v8, v9
	v_cvt_pk_f16_f32 v8, v6, v7
	v_cvt_pk_f16_f32 v7, v4, v5
	v_cvt_pk_f16_f32 v6, v2, v3
	v_cvt_pk_f16_f32 v5, v32, v33
	v_cvt_pk_f16_f32 v4, v30, v31
	v_mfma_f32_32x32x16_f16 v[34:49], v[22:25], v[6:9], 0
	v_cvt_pk_f16_f32 v3, v28, v29
	v_cvt_pk_f16_f32 v2, v26, v27
	v_cvt_pk_f16_f32 v9, v16, v17
	v_cvt_pk_f16_f32 v8, v14, v15
	v_cvt_pk_f16_f32 v7, v12, v13
	v_cvt_pk_f16_f32 v6, v10, v11
	v_mov_b32_e32 v67, v66
	s_nop 0
	v_mfma_f32_32x32x16_f16 v[18:33], v[2:5], v[6:9], 0
	s_nop 2
	v_max3_f32 v2, v34, v35, v36
	v_max3_f32 v2, v2, v37, v38
	s_nop 6
	v_max3_f32 v30, v2, v39, v40
	v_mfma_f32_32x32x16_f16 v[2:17], v[192:195], v[96:99], 0
	v_max_f32_e32 v31, v45, v45
	v_max_f32_e32 v32, v44, v44
	v_max3_f32 v30, v30, v41, v42
	v_max_f32_e32 v31, v32, v31
	v_max3_f32 v31, v30, v43, v31
	v_cndmask_b32_e64 v30, v30, v31, s[0:1]
	v_mov_b32_e32 v31, v30
	v_mfma_f32_32x32x16_f16 v[2:17], v[188:191], v[76:79], v[2:17]
	s_nop 0
	v_permlane32_swap_b32_e32 v30, v31
	v_max_f32_e32 v31, v31, v31
	v_max_f32_e32 v30, v30, v30
	v_max_f32_e32 v30, v30, v31
	v_sub_f32_e32 v31, v34, v30
	v_exp_f32_e32 v34, v31
	v_mfma_f32_32x32x16_f16 v[2:17], v[184:187], v[72:75], v[2:17]
	v_sub_f32_e32 v31, v35, v30
	v_sub_f32_e32 v33, v37, v30
	v_exp_f32_e32 v35, v31
	v_sub_f32_e32 v31, v36, v30
	v_exp_f32_e32 v36, v33
	v_sub_f32_e32 v33, v38, v30
	v_exp_f32_e32 v46, v33
	v_mfma_f32_32x32x16_f16 v[2:17], v[180:183], v[68:71], v[2:17]
	v_sub_f32_e32 v33, v39, v30
	v_sub_f32_e32 v37, v41, v30
	v_exp_f32_e32 v39, v33
	v_sub_f32_e32 v33, v40, v30
	v_exp_f32_e32 v40, v37
	v_sub_f32_e32 v37, v42, v30
	v_exp_f32_e32 v41, v37
	v_sub_f32_e32 v37, v43, v30
	v_exp_f32_e32 v37, v37
	v_mfma_f32_32x32x16_f16 v[2:17], v[176:179], v[92:95], v[2:17]
	v_exp_f32_e32 v31, v31
	v_add_f32_e32 v32, 0, v34
	v_cndmask_b32_e64 v42, v37, 0, s[14:15]
	v_sub_f32_e32 v37, v44, v30
	v_sub_f32_e32 v30, v45, v30
	v_exp_f32_e32 v30, v30
	v_add_f32_e32 v32, v35, v32
	v_mfma_f32_32x32x16_f16 v[2:17], v[172:175], v[84:87], v[2:17]
	v_add_f32_e32 v32, v31, v32
	v_cndmask_b32_e64 v44, v30, 0, s[14:15]
	v_cvt_pk_f16_f32 v30, v34, v35
	v_max3_f32 v34, v18, v19, v20
	v_max3_f32 v34, v34, v21, v22
	v_add_f32_e32 v32, v36, v32
	v_cvt_pk_f16_f32 v31, v31, v36
	v_max3_f32 v34, v34, v23, v24
	v_max_f32_e32 v35, v29, v29
	v_max_f32_e32 v36, v28, v28
	v_max3_f32 v34, v34, v25, v26
	v_max_f32_e32 v35, v36, v35
	v_max3_f32 v35, v34, v27, v35
	v_cndmask_b32_e64 v34, v34, v35, s[0:1]
	v_exp_f32_e32 v33, v33
	v_mov_b32_e32 v35, v34
	s_nop 1
	v_permlane32_swap_b32_e32 v34, v35
	v_add_f32_e32 v32, v46, v32
	v_mfma_f32_32x32x16_f16 v[2:17], v[168:171], v[88:91], v[2:17]
	v_max_f32_e32 v35, v35, v35
	v_max_f32_e32 v34, v34, v34
	v_add_f32_e32 v32, v39, v32
	v_exp_f32_e32 v37, v37
	v_max_f32_e32 v34, v34, v35
	v_add_f32_e32 v32, v33, v32
	v_sub_f32_e32 v18, v18, v34
	v_add_f32_e32 v32, v40, v32
	v_exp_f32_e32 v36, v18
	v_sub_f32_e32 v18, v19, v34
	v_sub_f32_e32 v19, v20, v34
	v_add_f32_e32 v32, v41, v32
	v_cvt_pk_f16_f32 v33, v33, v40
	v_exp_f32_e32 v40, v19
	v_sub_f32_e32 v19, v21, v34
	v_add_f32_e32 v32, v42, v32
	v_cndmask_b32_e64 v43, v37, 0, s[14:15]
	v_cvt_pk_f16_f32 v64, v41, v42
	v_exp_f32_e32 v41, v19
	v_sub_f32_e32 v19, v22, v34
	v_add_f32_e32 v32, v43, v32
	v_exp_f32_e32 v42, v19
	v_sub_f32_e32 v19, v23, v34
	v_add_f32_e32 v37, v44, v32
	v_cvt_pk_f16_f32 v65, v43, v44
	v_exp_f32_e32 v44, v19
	v_sub_f32_e32 v19, v24, v34
	v_mfma_f32_32x32x16_f16 v[2:17], v[164:167], v[80:83], v[2:17]
	v_cvt_pk_f16_f32 v32, v46, v39
	v_exp_f32_e32 v39, v18
	v_exp_f32_e32 v46, v19
	v_sub_f32_e32 v19, v25, v34
	v_exp_f32_e32 v47, v19
	v_sub_f32_e32 v19, v26, v34
	v_exp_f32_e32 v43, v19
	v_sub_f32_e32 v19, v27, v34
	v_add_f32_e32 v18, 0, v36
	v_exp_f32_e32 v19, v19
	v_add_f32_e32 v18, v39, v18
	v_add_f32_e32 v18, v40, v18
	v_add_f32_e32 v18, v41, v18
	v_add_f32_e32 v18, v42, v18
	v_cndmask_b32_e64 v45, v19, 0, s[14:15]
	v_sub_f32_e32 v19, v28, v34
	v_add_f32_e32 v18, v44, v18
	v_exp_f32_e32 v19, v19
	v_sub_f32_e32 v20, v29, v34
	v_cvt_pk_f16_f32 v9, v8, v9
	v_cvt_pk_f16_f32 v8, v6, v7
	v_cvt_pk_f16_f32 v7, v4, v5
	v_cvt_pk_f16_f32 v6, v2, v3
	v_add_f32_e32 v18, v46, v18
	v_exp_f32_e32 v20, v20
	v_add_f32_e32 v18, v47, v18
	v_add_f32_e32 v18, v43, v18
	v_add_f32_e32 v18, v45, v18
	v_cndmask_b32_e64 v48, v19, 0, s[14:15]
	v_add_f32_e32 v2, v48, v18
	v_cndmask_b32_e64 v49, v20, 0, s[14:15]
	v_cvt_pk_f16_f32 v35, v16, v17
	v_mfma_f32_32x32x16_f16 v[16:31], v[6:9], v[30:33], 0
	v_cvt_pk_f16_f32 v34, v14, v15
	v_cvt_pk_f16_f32 v33, v12, v13
	v_cvt_pk_f16_f32 v32, v10, v11
	v_add_f32_e32 v62, v49, v2
	v_mov_b32_e32 v38, v37
	v_mov_b32_e32 v63, v62
	s_nop 0
	v_permlane32_swap_b32_e32 v37, v38
	v_mfma_f32_32x32x16_f16 v[16:31], v[32:35], v[64:67], v[16:31]
	v_permlane32_swap_b32_e32 v62, v63
	s_and_saveexec_b64 s[2:3], s[4:5]
	s_cbranch_execz .LBB1_59
	v_add_f32_e32 v2, v37, v38
	v_rcp_f32_e32 v2, v2
	s_nop 6
	v_mov_b32_e32 v4, v17
	v_mov_b32_e32 v5, v18
	v_mov_b32_e32 v10, v21
	v_fma_mixlo_f16 v3, v2, v16, 0
	v_pk_mul_f32 v[4:5], v[2:3], v[4:5] op_sel_hi:[0,1]
	v_mov_b32_e32 v11, v22
	v_cvt_pk_f16_f32 v5, v4, v5
	v_pk_mul_f32 v[10:11], v[2:3], v[10:11] op_sel_hi:[0,1]
	v_fma_mixlo_f16 v12, v2, v20, 0
	v_pack_b32_f16 v4, v3, v5
	v_cvt_pk_f16_f32 v3, v10, v11
	v_fma_mixlo_f16 v11, v2, v19, 0
	v_fma_mixlo_f16 v2, v2, v23, 0
	v_pack_b32_f16 v10, v12, v3
	v_alignbit_b32 v5, v11, v5, 16
	v_alignbit_b32 v11, v2, v3, 16
	ds_write2_b64 v248, v[4:5], v[10:11] offset1:2
